# router workgroup-aggregated slot counters made robust to up to 16 tokens per wave (two-pass flush); otherwise as previous
# speedup vs baseline: 1.0147x; 1.0020x over previous
.LBB0_1619:
	s_or_b64 exec, exec, s[0:1]
	s_mov_b64 exec, 0xffff
	v_mbcnt_lo_u32_b32 v80, -1, 0
	v_mbcnt_hi_u32_b32 v80, -1, v80
	s_lshl_b32 s98, s91, 9
	s_add_i32 s98, s98, 0x10000
	v_lshl_add_u32 v80, v80, 5, s98
	v_mov_b32_e32 v81, 0xff
	ds_write_b32 v80, v81
	s_mov_b64 exec, -1
	s_lshl_b32 s0, s13, 3
	s_add_i32 s56, s0, s91
	s_cmpk_gt_i32 s56, 0x3fff
	s_waitcnt vmcnt(16) lgkmcnt(0)
	s_barrier
	s_cbranch_scc1 .LBB0_1624
	s_lshl_b32 s58, s12, 3
	s_add_u32 s68, s52, 0x300000
	s_addc_u32 s69, s53, 0
	s_add_u32 s70, s52, 0x380000
	s_addc_u32 s71, s53, 0
	s_add_u32 s2, s52, 0x420000
	s_addc_u32 s3, s53, 0
	s_add_u32 s4, s52, 0x440000
	s_addc_u32 s5, s53, 0
	s_ashr_i32 s57, s56, 31
	s_lshl_b64 s[0:1], s[56:57], 2
	s_add_u32 s8, s0, 0x400000
	v_and_b32_e32 v0, 63, v0
	s_addc_u32 s9, s1, 0
	s_lshl_b64 s[0:1], s[56:57], 12
	s_ashr_i32 s59, s58, 31
	v_lshl_or_b32 v18, v0, 3, s0
	v_mov_b32_e32 v19, s1
	s_lshl_b32 s0, s13, 4
	v_readlane_b32 s1, v254, 53
	v_cmp_eq_u32_e64 s[36:37], 0, v0
	v_lshl_add_u32 v25, v0, 4, 0
	s_lshl_b64 s[72:73], s[58:59], 2
	s_lshl_b64 s[76:77], s[58:59], 12
	s_add_i32 s66, s1, s0
	s_lshl_b32 s12, s12, 4
	s_lshl_b32 s99, s91, 9
	s_add_i32 s99, s99, 0x10000
	s_branch .LBB0_1622

.LBB0_1624:
	s_waitcnt lgkmcnt(0)
	s_barrier
	s_cmp_lg_u32 s91, 0
	s_cbranch_scc1 .Lrt_done
	s_mov_b32 s98, 0x10000
.Lrt_pass:
	v_mbcnt_lo_u32_b32 v6, -1, 0
	v_mbcnt_hi_u32_b32 v6, -1, v6
	v_lshl_add_u32 v7, v6, 5, s98
	ds_read_b128 v[80:83], v7
	ds_read_b64 v[84:85], v7 offset:16
	v_mov_b32_e32 v86, 0
	v_mov_b32_e32 v87, 0
	v_mov_b32_e32 v88, 0
	s_waitcnt lgkmcnt(0)
	v_cmp_eq_u32_e64 s[38:39], 0, v80
	v_cmp_eq_u32_e64 s[40:41], 0, v81
	s_nop 1
	s_bcnt1_i32_b64 s42, s[38:39]
	s_bcnt1_i32_b64 s43, s[40:41]
	v_mbcnt_lo_u32_b32 v89, s38, 0
	v_mbcnt_hi_u32_b32 v89, s39, v89
	v_mbcnt_lo_u32_b32 v90, s40, 0
	v_mbcnt_hi_u32_b32 v90, s41, v90
	v_add_u32_e32 v90, s42, v90
	v_cndmask_b32_e64 v86, v86, v89, s[38:39]
	v_cndmask_b32_e64 v87, v87, v90, s[40:41]
	s_add_i32 s42, s42, s43
	v_writelane_b32 v88, s42, 0
	v_cmp_eq_u32_e64 s[38:39], 1, v80
	v_cmp_eq_u32_e64 s[40:41], 1, v81
	s_nop 1
	s_bcnt1_i32_b64 s42, s[38:39]
	s_bcnt1_i32_b64 s43, s[40:41]
	v_mbcnt_lo_u32_b32 v89, s38, 0
	v_mbcnt_hi_u32_b32 v89, s39, v89
	v_mbcnt_lo_u32_b32 v90, s40, 0
	v_mbcnt_hi_u32_b32 v90, s41, v90
	v_add_u32_e32 v90, s42, v90
	v_cndmask_b32_e64 v86, v86, v89, s[38:39]
	v_cndmask_b32_e64 v87, v87, v90, s[40:41]
	s_add_i32 s42, s42, s43
	v_writelane_b32 v88, s42, 1
	v_cmp_eq_u32_e64 s[38:39], 2, v80
	v_cmp_eq_u32_e64 s[40:41], 2, v81
	s_nop 1
	s_bcnt1_i32_b64 s42, s[38:39]
	s_bcnt1_i32_b64 s43, s[40:41]
	v_mbcnt_lo_u32_b32 v89, s38, 0
	v_mbcnt_hi_u32_b32 v89, s39, v89
	v_mbcnt_lo_u32_b32 v90, s40, 0
	v_mbcnt_hi_u32_b32 v90, s41, v90
	v_add_u32_e32 v90, s42, v90
	v_cndmask_b32_e64 v86, v86, v89, s[38:39]
	v_cndmask_b32_e64 v87, v87, v90, s[40:41]
	s_add_i32 s42, s42, s43
	v_writelane_b32 v88, s42, 2
	v_cmp_eq_u32_e64 s[38:39], 3, v80
	v_cmp_eq_u32_e64 s[40:41], 3, v81
	s_nop 1
	s_bcnt1_i32_b64 s42, s[38:39]
	s_bcnt1_i32_b64 s43, s[40:41]
	v_mbcnt_lo_u32_b32 v89, s38, 0
	v_mbcnt_hi_u32_b32 v89, s39, v89
	v_mbcnt_lo_u32_b32 v90, s40, 0
	v_mbcnt_hi_u32_b32 v90, s41, v90
	v_add_u32_e32 v90, s42, v90
	v_cndmask_b32_e64 v86, v86, v89, s[38:39]
	v_cndmask_b32_e64 v87, v87, v90, s[40:41]
	s_add_i32 s42, s42, s43
	v_writelane_b32 v88, s42, 3
	v_cmp_eq_u32_e64 s[38:39], 4, v80
	v_cmp_eq_u32_e64 s[40:41], 4, v81
	s_nop 1
	s_bcnt1_i32_b64 s42, s[38:39]
	s_bcnt1_i32_b64 s43, s[40:41]
	v_mbcnt_lo_u32_b32 v89, s38, 0
	v_mbcnt_hi_u32_b32 v89, s39, v89
	v_mbcnt_lo_u32_b32 v90, s40, 0
	v_mbcnt_hi_u32_b32 v90, s41, v90
	v_add_u32_e32 v90, s42, v90
	v_cndmask_b32_e64 v86, v86, v89, s[38:39]
	v_cndmask_b32_e64 v87, v87, v90, s[40:41]
	s_add_i32 s42, s42, s43
	v_writelane_b32 v88, s42, 4
	v_cmp_eq_u32_e64 s[38:39], 5, v80
	v_cmp_eq_u32_e64 s[40:41], 5, v81
	s_nop 1
	s_bcnt1_i32_b64 s42, s[38:39]
	s_bcnt1_i32_b64 s43, s[40:41]
	v_mbcnt_lo_u32_b32 v89, s38, 0
	v_mbcnt_hi_u32_b32 v89, s39, v89
	v_mbcnt_lo_u32_b32 v90, s40, 0
	v_mbcnt_hi_u32_b32 v90, s41, v90
	v_add_u32_e32 v90, s42, v90
	v_cndmask_b32_e64 v86, v86, v89, s[38:39]
	v_cndmask_b32_e64 v87, v87, v90, s[40:41]
	s_add_i32 s42, s42, s43
	v_writelane_b32 v88, s42, 5
	v_cmp_eq_u32_e64 s[38:39], 6, v80
	v_cmp_eq_u32_e64 s[40:41], 6, v81
	s_nop 1
	s_bcnt1_i32_b64 s42, s[38:39]
	s_bcnt1_i32_b64 s43, s[40:41]
	v_mbcnt_lo_u32_b32 v89, s38, 0
	v_mbcnt_hi_u32_b32 v89, s39, v89
	v_mbcnt_lo_u32_b32 v90, s40, 0
	v_mbcnt_hi_u32_b32 v90, s41, v90
	v_add_u32_e32 v90, s42, v90
	v_cndmask_b32_e64 v86, v86, v89, s[38:39]
	v_cndmask_b32_e64 v87, v87, v90, s[40:41]
	s_add_i32 s42, s42, s43
	v_writelane_b32 v88, s42, 6
	v_cmp_eq_u32_e64 s[38:39], 7, v80
	v_cmp_eq_u32_e64 s[40:41], 7, v81
	s_nop 1
	s_bcnt1_i32_b64 s42, s[38:39]
	s_bcnt1_i32_b64 s43, s[40:41]
	v_mbcnt_lo_u32_b32 v89, s38, 0
	v_mbcnt_hi_u32_b32 v89, s39, v89
	v_mbcnt_lo_u32_b32 v90, s40, 0
	v_mbcnt_hi_u32_b32 v90, s41, v90
	v_add_u32_e32 v90, s42, v90
	v_cndmask_b32_e64 v86, v86, v89, s[38:39]
	v_cndmask_b32_e64 v87, v87, v90, s[40:41]
	s_add_i32 s42, s42, s43
	v_writelane_b32 v88, s42, 7
	s_mov_b64 exec, 0xff
	v_mul_u32_u24_e32 v91, 0x2100, v6
	global_atomic_add v92, v91, v88, s[52:53] offset:384 sc0
	s_mov_b64 exec, -1
	v_lshlrev_b32_e32 v93, 2, v80
	v_lshlrev_b32_e32 v94, 2, v81
	s_add_u32 s20, s52, 0x300000
	s_addc_u32 s21, s53, 0
	s_add_u32 s22, s52, 0x380000
	s_addc_u32 s23, s53, 0
	s_add_u32 s44, s52, 0x400000
	s_addc_u32 s45, s53, 0
	s_add_u32 s46, s52, 0x420000
	s_addc_u32 s47, s53, 0
	s_add_u32 s48, s52, 0x440000
	s_addc_u32 s49, s53, 0
	s_waitcnt vmcnt(0)
	ds_bpermute_b32 v93, v93, v92
	ds_bpermute_b32 v94, v94, v92
	v_cmp_ne_u32_e32 vcc, 0xff, v80
	s_waitcnt lgkmcnt(0)
	v_add_u32_e32 v93, v93, v86
	v_add_u32_e32 v94, v94, v87
	s_and_saveexec_b64 s[38:39], vcc
	s_cbranch_execz .Lrt_nostore
	v_lshl_add_u32 v100, v80, 14, v93
	v_lshl_add_u32 v101, v81, 14, v94
	v_lshlrev_b32_e32 v97, 2, v100
	v_lshlrev_b32_e32 v98, 2, v101
	v_lshlrev_b32_e32 v95, 2, v85
	v_lshlrev_b32_e32 v96, 3, v85
	v_mov_b32_e32 v102, v83
	v_mov_b32_e32 v103, v84
	global_store_dword v95, v82, s[44:45]
	global_store_dwordx2 v96, v[102:103], s[48:49]
	global_store_dword v97, v85, s[20:21]
	global_store_dword v98, v85, s[20:21]
	global_store_dword v97, v82, s[22:23]
	global_store_dword v98, v82, s[22:23]
	global_store_dwordx2 v96, v[100:101], s[46:47]
.Lrt_nostore:
	s_or_b64 exec, exec, s[38:39]
	s_add_i32 s98, s98, 0x800
	s_cmp_lt_u32 s98, 0x11000
	s_cbranch_scc1 .Lrt_pass
